# address precompute: P10 gate block row-1 base computed early so all 16 gate-vector loads issue at one point
# baseline (speedup 1.0000x reference)
.LBB0_2510:
	s_cmp_lg_u32 s0, s38
	s_cselect_b64 s[36:37], -1, 0
	s_min_i32 s1, s38, 0x4000
	s_lshr_b32 s1, s1, 12
	s_mul_i32 s2, s1, 0x3000
	s_ashr_i32 s3, s2, 31
	s_lshl_b64 s[44:45], s[2:3], 2
	s_add_u32 s2, s8, s44
	s_addc_u32 s3, s9, s45
	v_lshlrev_b32_e32 v146, 16, v100
	v_and_b32_e32 v147, 0xffff0000, v100
	v_lshlrev_b32_e32 v148, 16, v101
	v_and_b32_e32 v149, 0xffff0000, v101
	v_lshlrev_b32_e32 v138, 16, v96
	v_and_b32_e32 v139, 0xffff0000, v96
	v_lshlrev_b32_e32 v140, 16, v97
	v_and_b32_e32 v141, 0xffff0000, v97
	v_lshlrev_b32_e32 v130, 16, v94
	v_and_b32_e32 v131, 0xffff0000, v94
	v_lshlrev_b32_e32 v132, 16, v95
	v_and_b32_e32 v133, 0xffff0000, v95
	v_lshlrev_b32_e32 v100, 16, v90
	v_and_b32_e32 v101, 0xffff0000, v90
	v_lshlrev_b32_e32 v116, 16, v91
	v_and_b32_e32 v117, 0xffff0000, v91
	v_lshlrev_b32_e32 v94, 16, v88
	v_and_b32_e32 v95, 0xffff0000, v88
	v_lshlrev_b32_e32 v96, 16, v89
	v_and_b32_e32 v97, 0xffff0000, v89
	v_lshlrev_b32_e32 v88, 16, v84
	v_and_b32_e32 v89, 0xffff0000, v84
	v_lshlrev_b32_e32 v90, 16, v85
	v_and_b32_e32 v91, 0xffff0000, v85
	v_lshl_add_u64 v[84:85], s[2:3], 0, v[2:3]
	s_mov_b64 s[2:3], 0xa000
	v_lshl_add_u64 v[154:155], v[84:85], 0, s[2:3]
	v_add_co_u32_e32 v84, vcc, s63, v84
	s_min_i32 s0, s0, 0x4000
	s_nop 0
	v_addc_co_u32_e32 v85, vcc, 0, v85, vcc
	s_lshr_b32 s0, s0, 12
	s_mulk_i32 s0, 0x3000
	s_ashr_i32 s1, s0, 31
	s_lshl_b64 s[46:47], s[0:1], 2
	s_add_u32 s0, s8, s46
	s_addc_u32 s1, s9, s47
	v_lshlrev_b32_e32 v142, 16, v114
	v_and_b32_e32 v143, 0xffff0000, v114
	v_lshl_add_u64 v[164:165], s[0:1], 0, v[2:3]
	v_lshlrev_b32_e32 v144, 16, v115
	v_and_b32_e32 v145, 0xffff0000, v115
	v_lshlrev_b32_e32 v134, 16, v112
	v_and_b32_e32 v135, 0xffff0000, v112
	v_lshlrev_b32_e32 v136, 16, v113
	v_and_b32_e32 v137, 0xffff0000, v113
	v_lshl_add_u64 v[166:167], v[164:165], 0, s[2:3]
	v_add_co_u32_e32 v194, vcc, s63, v164
	s_nop 1
	v_addc_co_u32_e32 v195, vcc, 0, v165, vcc
	global_load_dwordx4 v[168:171], v[84:85], off offset:-4096
	global_load_dwordx4 v[172:175], v[194:195], off offset:-4096
	global_load_dwordx4 v[176:179], v[154:155], off offset:1024
	global_load_dwordx4 v[180:183], v[166:167], off offset:1024
	global_load_dwordx4 v[184:187], v[154:155], off offset:2048
	global_load_dwordx4 v[190:193], v[166:167], off offset:2048
	global_load_dwordx4 v[212:215], v[154:155], off offset:3072
	global_load_dwordx4 v[216:219], v[166:167], off offset:3072
	global_load_dwordx4 v[224:227], v[84:85], off
	global_load_dwordx4 v[228:231], v[194:195], off
	global_load_dwordx4 v[232:235], v[84:85], off offset:1024
	global_load_dwordx4 v[236:239], v[194:195], off offset:1024
	global_load_dwordx4 v[240:243], v[84:85], off offset:2048
	global_load_dwordx4 v[244:247], v[194:195], off offset:2048
	global_load_dwordx4 v[248:251], v[84:85], off offset:3072
	v_lshlrev_b32_e32 v126, 16, v110
	v_and_b32_e32 v127, 0xffff0000, v110
	v_lshlrev_b32_e32 v128, 16, v111
	v_and_b32_e32 v129, 0xffff0000, v111
	v_lshlrev_b32_e32 v118, 16, v108
	v_and_b32_e32 v119, 0xffff0000, v108
	v_lshlrev_b32_e32 v120, 16, v109
	v_and_b32_e32 v121, 0xffff0000, v109
	v_lshlrev_b32_e32 v122, 16, v92
	v_and_b32_e32 v123, 0xffff0000, v92
	v_lshlrev_b32_e32 v124, 16, v93
	v_and_b32_e32 v125, 0xffff0000, v93
	v_lshlrev_b32_e32 v112, 16, v106
	v_and_b32_e32 v113, 0xffff0000, v106
	v_lshlrev_b32_e32 v114, 16, v107
	v_and_b32_e32 v115, 0xffff0000, v107
	v_lshlrev_b32_e32 v108, 16, v104
	v_and_b32_e32 v109, 0xffff0000, v104
	v_lshlrev_b32_e32 v110, 16, v105
	v_and_b32_e32 v111, 0xffff0000, v105
	v_lshlrev_b32_e32 v104, 16, v102
	v_and_b32_e32 v105, 0xffff0000, v102
	v_lshlrev_b32_e32 v106, 16, v103
	v_and_b32_e32 v107, 0xffff0000, v103
	v_lshlrev_b32_e32 v92, 16, v86
	v_and_b32_e32 v93, 0xffff0000, v86
	v_lshlrev_b32_e32 v102, 16, v98
	v_and_b32_e32 v103, 0xffff0000, v98
	v_lshlrev_b32_e32 v98, 16, v99
	v_and_b32_e32 v99, 0xffff0000, v99
	v_lshlrev_b32_e32 v86, 16, v87
	v_and_b32_e32 v87, 0xffff0000, v87
	v_readlane_b32 s2, v253, 48
	v_readlane_b32 s3, v253, 49
	s_mov_b64 s[0:1], -1
	s_waitcnt vmcnt(14)
	v_mov_b32_e32 v150, v168
	v_mov_b32_e32 v151, v169
	v_mov_b32_e32 v152, v170
	v_mov_b32_e32 v153, v171
	global_load_dwordx4 v[168:171], v[194:195], off offset:3072
	v_pk_fma_f32 v[64:65], v[150:151], v[64:65], v[142:143]
	v_pk_fma_f32 v[66:67], v[152:153], v[66:67], v[144:145]
	s_nop 0
	s_and_b64 vcc, exec, s[2:3]
	s_waitcnt vmcnt(14)
	v_mov_b32_e32 v150, v172
	v_mov_b32_e32 v151, v173
	v_mov_b32_e32 v152, v174
	v_mov_b32_e32 v153, v175
	v_pk_fma_f32 v[60:61], v[150:151], v[60:61], v[146:147]
	v_pk_fma_f32 v[62:63], v[152:153], v[62:63], v[148:149]
	s_waitcnt vmcnt(13)
	v_mov_b32_e32 v144, v176
	v_mov_b32_e32 v145, v177
	v_mov_b32_e32 v146, v178
	v_mov_b32_e32 v147, v179
	v_pk_fma_f32 v[56:57], v[144:145], v[56:57], v[134:135]
	v_pk_fma_f32 v[58:59], v[146:147], v[58:59], v[136:137]
	s_waitcnt vmcnt(12)
	v_mov_b32_e32 v134, v180
	v_mov_b32_e32 v135, v181
	v_mov_b32_e32 v136, v182
	v_mov_b32_e32 v137, v183
	v_pk_fma_f32 v[52:53], v[134:135], v[52:53], v[138:139]
	v_pk_fma_f32 v[54:55], v[136:137], v[54:55], v[140:141]
	s_waitcnt vmcnt(11)
	v_mov_b32_e32 v134, v184
	v_mov_b32_e32 v135, v185
	v_mov_b32_e32 v136, v186
	v_mov_b32_e32 v137, v187
	v_pk_fma_f32 v[48:49], v[134:135], v[48:49], v[126:127]
	v_pk_fma_f32 v[50:51], v[136:137], v[50:51], v[128:129]
	s_waitcnt vmcnt(10)
	v_mov_b32_e32 v126, v190
	v_mov_b32_e32 v127, v191
	v_mov_b32_e32 v128, v192
	v_mov_b32_e32 v129, v193
	v_pk_fma_f32 v[44:45], v[126:127], v[44:45], v[130:131]
	v_pk_fma_f32 v[46:47], v[128:129], v[46:47], v[132:133]
	s_waitcnt vmcnt(9)
	v_mov_b32_e32 v126, v212
	v_mov_b32_e32 v127, v213
	v_mov_b32_e32 v128, v214
	v_mov_b32_e32 v129, v215
	v_pk_fma_f32 v[40:41], v[126:127], v[40:41], v[118:119]
	v_pk_fma_f32 v[42:43], v[128:129], v[42:43], v[120:121]
	v_mul_f32_e32 v140, v40, v40
	v_mul_f32_e32 v138, v42, v42
	s_waitcnt vmcnt(8)
	v_mov_b32_e32 v118, v216
	v_mov_b32_e32 v119, v217
	v_mov_b32_e32 v120, v218
	v_mov_b32_e32 v121, v219
	v_pk_fma_f32 v[36:37], v[118:119], v[36:37], v[122:123]
	v_pk_fma_f32 v[38:39], v[120:121], v[38:39], v[124:125]
	s_waitcnt vmcnt(7)
	v_mov_b32_e32 v118, v224
	v_mov_b32_e32 v119, v225
	v_mov_b32_e32 v120, v226
	v_mov_b32_e32 v121, v227
	v_pk_fma_f32 v[34:35], v[120:121], v[34:35], v[114:115]
	v_pk_fma_f32 v[32:33], v[118:119], v[32:33], v[112:113]
	v_mul_f32_e32 v128, v32, v32
	v_mul_f32_e32 v132, v33, v33
	v_mul_f32_e32 v124, v34, v34
	v_mul_f32_e32 v126, v35, v35
	s_waitcnt vmcnt(6)
	v_mov_b32_e32 v112, v228
	v_mov_b32_e32 v113, v229
	v_mov_b32_e32 v114, v230
	v_mov_b32_e32 v115, v231
	v_pk_fma_f32 v[30:31], v[114:115], v[30:31], v[116:117]
	v_pk_fma_f32 v[28:29], v[112:113], v[28:29], v[100:101]
	s_waitcnt vmcnt(5)
	v_mov_b32_e32 v112, v232
	v_mov_b32_e32 v113, v233
	v_mov_b32_e32 v114, v234
	v_mov_b32_e32 v115, v235
	v_pk_fma_f32 v[26:27], v[114:115], v[26:27], v[110:111]
	v_pk_fma_f32 v[24:25], v[112:113], v[24:25], v[108:109]
	v_pk_mul_f32 v[136:137], v[24:25], v[24:25]
	v_pk_mul_f32 v[114:115], v[44:45], v[44:45]
	v_mul_f32_e32 v112, v36, v36
	s_waitcnt vmcnt(4)
	v_mov_b32_e32 v108, v236
	v_mov_b32_e32 v109, v237
	v_mov_b32_e32 v110, v238
	v_mov_b32_e32 v111, v239
	v_pk_fma_f32 v[22:23], v[110:111], v[22:23], v[96:97]
	v_pk_fma_f32 v[20:21], v[108:109], v[20:21], v[94:95]
	v_mul_f32_e32 v110, v38, v38
	v_pk_mul_f32 v[108:109], v[20:21], v[20:21]
	s_waitcnt vmcnt(3)
	v_mov_b32_e32 v94, v240
	v_mov_b32_e32 v95, v241
	v_mov_b32_e32 v96, v242
	v_mov_b32_e32 v97, v243
	v_pk_fma_f32 v[18:19], v[96:97], v[18:19], v[106:107]
	v_pk_fma_f32 v[16:17], v[94:95], v[16:17], v[104:105]
	v_mul_f32_e32 v104, v28, v28
	v_mul_f32_e32 v106, v29, v29
	v_mul_f32_e32 v134, v16, v16
	v_mul_f32_e32 v130, v18, v18
	s_waitcnt vmcnt(2)
	v_mov_b32_e32 v94, v244
	v_mov_b32_e32 v95, v245
	v_mov_b32_e32 v96, v246
	v_mov_b32_e32 v97, v247
	v_pk_fma_f32 v[12:13], v[94:95], v[12:13], v[92:93]
	v_pk_fma_f32 v[14:15], v[96:97], v[14:15], v[86:87]
	v_mul_f32_e32 v96, v30, v30
	v_mul_f32_e32 v100, v14, v14
	s_waitcnt vmcnt(1)
	v_mov_b32_e32 v92, v248
	v_mov_b32_e32 v93, v249
	v_mov_b32_e32 v94, v250
	v_mov_b32_e32 v95, v251
	v_pk_fma_f32 v[84:85], v[94:95], v[10:11], v[98:99]
	v_pk_fma_f32 v[86:87], v[92:93], v[8:9], v[102:103]
	v_mul_f32_e32 v120, v86, v86
	v_mul_f32_e32 v122, v87, v87
	v_mul_f32_e32 v116, v84, v84
	v_mul_f32_e32 v118, v85, v85
	v_mul_f32_e32 v98, v31, v31
	v_pk_mul_f32 v[142:143], v[48:49], v[48:49]
	v_mul_f32_e32 v102, v12, v12
	s_waitcnt vmcnt(0)
	v_mov_b32_e32 v8, v168
	v_mov_b32_e32 v9, v169
	v_mov_b32_e32 v10, v170
	v_mov_b32_e32 v11, v171
	v_pk_fma_f32 v[10:11], v[10:11], v[6:7], v[90:91]
	v_pk_fma_f32 v[8:9], v[8:9], v[4:5], v[88:89]
	v_cndmask_b32_e64 v4, 0, 1, s[36:37]
	v_mul_f32_e32 v92, v8, v8
	v_mul_f32_e32 v94, v9, v9
	v_mul_f32_e32 v88, v10, v10
	v_mul_f32_e32 v90, v11, v11
	v_cmp_ne_u32_e64 s[36:37], 1, v4
	s_cbranch_vccz .LBB0_2528
	v_mov_b32_e32 v6, v65
	v_mov_b32_e32 v7, v57
	v_mov_b32_e32 v146, v67
	v_mov_b32_e32 v147, v59
	v_mov_b32_e32 v4, v64
	v_mov_b32_e32 v5, v56
	v_pk_mul_f32 v[6:7], v[6:7], v[6:7]
	v_mov_b32_e32 v144, v66
	v_mov_b32_e32 v145, v58
	v_pk_mul_f32 v[146:147], v[146:147], v[146:147]
	v_pk_fma_f32 v[4:5], v[4:5], v[4:5], v[6:7]
	v_pk_fma_f32 v[6:7], v[144:145], v[144:145], v[146:147]
	v_mov_b32_e32 v144, v142
	v_pk_add_f32 v[4:5], v[4:5], v[6:7]
	v_pk_mul_f32 v[6:7], v[50:51], v[50:51]
	v_pk_add_f32 v[4:5], v[4:5], v[4:5] op_sel_hi:[0,1]
	v_mov_b32_e32 v145, v7
	v_pk_mov_b32 v[6:7], v[142:143], v[6:7] op_sel:[1,0]
	v_pk_fma_f32 v[146:147], v[42:43], v[42:43], v[138:139] op_sel_hi:[1,1,0]
	v_pk_add_f32 v[6:7], v[6:7], v[144:145]
	v_pk_fma_f32 v[144:145], v[40:41], v[40:41], v[140:141] op_sel_hi:[1,1,0]
	v_pk_add_f32 v[6:7], v[6:7], v[6:7] op_sel_hi:[0,1]
	v_mov_b32_e32 v129, v145
	v_mov_b32_e32 v133, v147
	v_mov_b32_e32 v125, v7
	v_mov_b32_e32 v127, v5
	v_pk_add_f32 v[144:145], v[128:129], v[132:133]
	v_pk_add_f32 v[4:5], v[124:125], v[126:127]
	v_pk_mul_f32 v[6:7], v[26:27], v[26:27]
	v_pk_add_f32 v[4:5], v[144:145], v[4:5]
	v_mov_b32_e32 v144, v136
	v_mov_b32_e32 v145, v7
	v_pk_mov_b32 v[6:7], v[136:137], v[6:7] op_sel:[1,0]
	v_pk_add_f32 v[4:5], v[4:5], v[4:5] op_sel_hi:[0,1]
	v_pk_add_f32 v[6:7], v[6:7], v[144:145]
	v_pk_fma_f32 v[144:145], v[16:17], v[16:17], v[134:135] op_sel_hi:[1,1,0]
	v_pk_add_f32 v[6:7], v[6:7], v[6:7] op_sel_hi:[0,1]
	v_pk_fma_f32 v[146:147], v[18:19], v[18:19], v[130:131] op_sel_hi:[1,1,0]
	v_mov_b32_e32 v121, v145
	v_mov_b32_e32 v123, v147
	v_mov_b32_e32 v117, v7
	v_mov_b32_e32 v119, v5
	v_pk_add_f32 v[144:145], v[120:121], v[122:123]
	v_pk_add_f32 v[4:5], v[116:117], v[118:119]
	v_mov_b32_e32 v6, v61
	v_pk_add_f32 v[146:147], v[144:145], v[4:5]
	v_and_b32_e32 v5, 64, v207
	v_xor_b32_e32 v4, 16, v207
	v_add_u32_e32 v101, 64, v5
	v_cmp_lt_i32_e32 vcc, v4, v101
	v_mov_b32_e32 v7, v53
	v_mov_b32_e32 v148, v63
	v_cndmask_b32_e32 v4, v207, v4, vcc
	v_mov_b32_e32 v149, v55
	v_lshlrev_b32_e32 v103, 2, v4
	v_mov_b32_e32 v4, v60
	v_mov_b32_e32 v5, v52
	v_pk_mul_f32 v[6:7], v[6:7], v[6:7]
	v_mov_b32_e32 v144, v62
	v_mov_b32_e32 v145, v54
	v_pk_mul_f32 v[148:149], v[148:149], v[148:149]
	v_pk_fma_f32 v[4:5], v[4:5], v[4:5], v[6:7]
	v_pk_fma_f32 v[6:7], v[144:145], v[144:145], v[148:149]
	v_pk_fma_f32 v[152:153], v[36:37], v[36:37], v[112:113] op_sel_hi:[1,1,0]
	v_pk_add_f32 v[4:5], v[4:5], v[6:7]
	v_mov_b32_e32 v7, s65
	ds_read_b64 v[144:145], v7
	v_pk_add_f32 v[148:149], v[4:5], v[4:5] op_sel_hi:[0,1]
	v_pk_mul_f32 v[4:5], v[46:47], v[46:47]
	v_mov_b32_e32 v6, v114
	v_mov_b32_e32 v7, v5
	v_pk_mov_b32 v[4:5], v[114:115], v[4:5] op_sel:[1,0]
	s_waitcnt lgkmcnt(0)
	v_readfirstlane_b32 s0, v144
	v_pk_add_f32 v[4:5], v[4:5], v[6:7]
	v_readfirstlane_b32 s1, v145
	v_pk_add_f32 v[150:151], v[4:5], v[4:5] op_sel_hi:[0,1]
	v_pk_fma_f32 v[154:155], v[38:39], v[38:39], v[110:111] op_sel_hi:[1,1,0]
	v_mov_b32_e32 v105, v153
	v_mov_b32_e32 v107, v155
	v_mov_b32_e32 v97, v151
	global_load_dwordx4 v[4:7], v2, s[0:1]
	v_mov_b32_e32 v99, v149
	v_pk_add_f32 v[152:153], v[104:105], v[106:107]
	v_pk_add_f32 v[148:149], v[96:97], v[98:99]
	v_pk_mul_f32 v[150:151], v[22:23], v[22:23]
	v_pk_add_f32 v[148:149], v[152:153], v[148:149]
	v_mov_b32_e32 v152, v108
	v_mov_b32_e32 v153, v151
	v_pk_mov_b32 v[150:151], v[108:109], v[150:151] op_sel:[1,0]
	v_pk_add_f32 v[148:149], v[148:149], v[148:149] op_sel_hi:[0,1]
	v_pk_add_f32 v[150:151], v[150:151], v[152:153]
	v_pk_fma_f32 v[152:153], v[12:13], v[12:13], v[102:103] op_sel_hi:[1,1,0]
	v_pk_add_f32 v[150:151], v[150:151], v[150:151] op_sel_hi:[0,1]
	v_pk_fma_f32 v[154:155], v[14:15], v[14:15], v[100:101] op_sel_hi:[1,1,0]
	v_mov_b32_e32 v93, v153
	v_mov_b32_e32 v95, v155
	v_mov_b32_e32 v89, v151
	v_mov_b32_e32 v91, v149
	v_pk_add_f32 v[152:153], v[92:93], v[94:95]
	v_pk_add_f32 v[148:149], v[88:89], v[90:91]
	v_mov_b32_e32 v151, v146
	v_pk_add_f32 v[148:149], v[152:153], v[148:149]
	v_xor_b32_e32 v89, 32, v207
	v_mov_b32_e32 v150, v148
	v_mov_b32_e32 v146, v149
	v_pk_add_f32 v[146:147], v[150:151], v[146:147]
	v_cmp_lt_i32_e32 vcc, v89, v101
	s_mov_b32 s0, 0x3a000000
	v_mov_b32_dpp v149, v147 quad_perm:[1,0,3,2] row_mask:0xf bank_mask:0xf bound_ctrl:1
	v_mov_b32_dpp v148, v146 quad_perm:[1,0,3,2] row_mask:0xf bank_mask:0xf bound_ctrl:1
	v_pk_add_f32 v[146:147], v[146:147], v[148:149]
	v_cndmask_b32_e32 v89, v207, v89, vcc
	v_lshlrev_b32_e32 v89, 2, v89
	v_mov_b32_dpp v149, v147 quad_perm:[2,3,0,1] row_mask:0xf bank_mask:0xf bound_ctrl:1
	v_mov_b32_dpp v148, v146 quad_perm:[2,3,0,1] row_mask:0xf bank_mask:0xf bound_ctrl:1
	v_pk_add_f32 v[146:147], v[146:147], v[148:149]
	s_nop 1
	v_mov_b32_dpp v149, v147 row_half_mirror row_mask:0xf bank_mask:0xf bound_ctrl:1
	v_mov_b32_dpp v148, v146 row_half_mirror row_mask:0xf bank_mask:0xf bound_ctrl:1
	v_pk_add_f32 v[146:147], v[146:147], v[148:149]
	s_nop 1
	v_mov_b32_dpp v149, v147 row_mirror row_mask:0xf bank_mask:0xf bound_ctrl:1
	v_mov_b32_dpp v148, v146 row_mirror row_mask:0xf bank_mask:0xf bound_ctrl:1
	v_pk_add_f32 v[146:147], v[146:147], v[148:149]
	ds_bpermute_b32 v149, v103, v147
	ds_bpermute_b32 v148, v103, v146
	s_waitcnt lgkmcnt(0)
	v_pk_add_f32 v[146:147], v[146:147], v[148:149]
	ds_bpermute_b32 v149, v89, v147
	ds_bpermute_b32 v148, v89, v146
	s_waitcnt lgkmcnt(0)
	v_pk_add_f32 v[146:147], v[146:147], v[148:149]
	s_nop 0
	v_pk_fma_f32 v[146:147], v[146:147], s[0:1], v[188:189] op_sel_hi:[1,0,0]
	s_nop 0
	v_mul_f32_e32 v89, 0x4b800000, v147
	v_cmp_gt_f32_e32 vcc, s11, v147
	v_mul_f32_e32 v91, 0x4b800000, v146
	v_cmp_gt_f32_e64 s[0:1], s11, v146
	v_cndmask_b32_e32 v89, v147, v89, vcc
	v_rsq_f32_e32 v89, v89
	v_cndmask_b32_e64 v91, v146, v91, s[0:1]
	v_rsq_f32_e32 v91, v91
	v_mul_f32_e32 v93, 0x45800000, v89
	v_cndmask_b32_e32 v150, v89, v93, vcc
	v_mul_f32_e32 v89, 0x45800000, v91
	v_cndmask_b32_e64 v148, v91, v89, s[0:1]
	s_lshl_b64 s[0:1], s[42:43], 2
	s_add_u32 s0, s16, s0
	s_addc_u32 s1, s17, s1
	s_lshl_b64 s[2:3], s[40:41], 2
	s_add_u32 s2, s16, s2
	s_addc_u32 s3, s17, s3
	v_pk_mul_f32 v[152:153], v[150:151], v[64:65] op_sel_hi:[0,1]
	v_pk_mul_f32 v[154:155], v[150:151], v[66:67] op_sel_hi:[0,1]
	v_mov_b32_e32 v149, v148
	v_lshl_add_u64 v[146:147], s[2:3], 0, v[2:3]
	s_waitcnt vmcnt(0)
	v_pk_mul_f32 v[154:155], v[154:155], v[6:7]
	v_pk_mul_f32 v[152:153], v[152:153], v[4:5]
	s_and_b64 vcc, exec, s[36:37]
	global_store_dwordx4 v2, v[152:155], s[0:1]
	s_cbranch_vccnz .LBB0_2513
	s_nop 0
	v_mov_b32_e32 v152, v148
	v_mov_b32_e32 v153, v148
	v_pk_mul_f32 v[152:153], v[152:153], v[62:63]
	v_pk_mul_f32 v[154:155], v[148:149], v[60:61]
	v_pk_mul_f32 v[6:7], v[152:153], v[6:7]
	v_pk_mul_f32 v[4:5], v[154:155], v[4:5]
	global_store_dwordx4 v[146:147], v[4:7], off
